# speedup vs baseline: 1.0206x; 1.0206x over previous
.LBB0_36:
	s_endpgm
	.p2align	8

_ZN12_GLOBAL__N_113search_kernelEPKfS1_PhPf:
	s_load_dwordx2 s[8:9], s[0:1], 0x0
	s_load_dwordx2 s[4:5], s[0:1], 0x10
	s_movk_i32 s3, 0x90
	v_readfirstlane_b32 s10, v0
	v_cmp_gt_u32_e32 vcc, s3, v0
	s_and_saveexec_b64 s[6:7], vcc
	v_mov_b32_e32 v2, -1
	v_lshlrev_b32_e32 v1, 3, v0
	v_mov_b32_e32 v3, v2
	ds_write_b64 v1, v[2:3] offset:16384
	s_or_b64 exec, exec, s[6:7]
	s_waitcnt lgkmcnt(0)
	s_add_u32 s6, s4, 0x240000
	s_addc_u32 s7, s5, 0
	s_lshl_b32 s11, s2, 1
	s_and_b32 s14, s11, 14
	s_ashr_i32 s11, s2, 7
	s_lshr_b32 s15, s10, 6
	s_add_i32 s14, s14, s11
	s_bfe_u32 s2, s2, 0x40003
	s_mul_i32 s11, s15, 24
	v_mul_u32_u24_e32 v2, 0x71d, v0
	v_mul_u32_u24_e32 v4, 0x195, v0
	s_min_u32 s18, s11, 0xa5
	s_mul_i32 s11, s14, 3
	s_mul_i32 s12, s2, 9
	s_mov_b32 s13, 0
	v_lshrrev_b32_e32 v3, 16, v2
	s_movk_i32 s19, 0xffdc
	v_lshrrev_b32_e32 v5, 17, v4
	v_mad_i32_i24 v2, v3, s19, v0
	v_mad_i32_i24 v4, v5, -9, v3
	v_add_u32_e32 v3, s11, v5
	v_mov_b64_e32 v[6:7], s[12:13]
	v_mad_i64_i32 v[8:9], s[16:17], v3, s3, v[6:7]
	v_ashrrev_i32_e32 v5, 31, v4
	v_lshl_add_u64 v[4:5], v[8:9], 0, v[4:5]
	s_movk_i32 s13, 0x240
	v_mov_b64_e32 v[8:9], s[8:9]
	v_mad_u64_u32 v[10:11], s[8:9], v4, s13, v[8:9]
	v_min_u32_e32 v4, 0x1cb, v0
	v_or_b32_e32 v4, 0x200, v4
	v_mad_i32_i24 v11, v5, s13, v11
	v_mul_u32_u24_e32 v5, 0x71d, v4
	v_ashrrev_i32_e32 v3, 31, v2
	v_lshrrev_b32_e32 v5, 16, v5
	v_lshl_add_u64 v[2:3], v[2:3], 4, v[10:11]
	v_mad_i32_i24 v10, v5, s19, v4
	v_mul_u32_u24_e32 v4, 0x653, v4
	v_lshrrev_b32_e32 v11, 19, v4
	v_mad_i32_i24 v4, v11, -9, v5
	v_add_u32_e32 v5, s11, v11
	v_mad_i64_i32 v[6:7], s[8:9], v5, s3, v[6:7]
	v_ashrrev_i32_e32 v5, 31, v4
	v_lshl_add_u64 v[4:5], v[6:7], 0, v[4:5]
	v_mad_u64_u32 v[12:13], s[8:9], v4, s13, v[8:9]
	s_mul_i32 s8, s14, 0x90
	s_barrier
	global_load_dwordx4 v[6:9], v[2:3], off
	s_add_i32 s3, s8, s12
	v_and_b32_e32 v210, 15, v0
	v_lshlrev_b32_e32 v252, 3, v210
	v_bfe_u32 v253, v0, 4, 2
	s_lshl_b32 s11, s3, 6
	v_and_b32_e32 v2, 48, v0
	s_mul_i32 s9, s14, 0xbd
	v_or3_b32 v2, s11, v2, v210
	s_add_i32 s18, s18, s9
	v_and_b32_e32 v1, 63, v0
	v_ashrrev_i32_e32 v3, 31, v2
	s_lshl_b32 s3, s18, 6
	v_mad_i32_i24 v13, v5, s13, v13
	v_lshl_add_u64 v[14:15], v[2:3], 4, s[4:5]
	v_or_b32_e32 v2, s3, v1
	v_ashrrev_i32_e32 v11, 31, v10
	v_ashrrev_i32_e32 v3, 31, v2
	v_lshl_add_u64 v[10:11], v[10:11], 4, v[12:13]
	v_lshl_add_u64 v[16:17], v[2:3], 4, s[6:7]
	global_load_dwordx4 v[2:5], v[14:15], off
	global_load_dwordx4 v[58:61], v[16:17], off nt
	s_add_i32 s12, s3, 64
	global_load_dwordx4 v[10:13], v[10:11], off
	v_or_b32_e32 v14, s12, v1
	v_ashrrev_i32_e32 v15, 31, v14
	v_lshl_add_u64 v[14:15], v[14:15], 4, s[6:7]
	s_add_i32 s12, s3, 0x80
	global_load_dwordx4 v[54:57], v[14:15], off nt
	v_or_b32_e32 v14, s12, v1
	v_ashrrev_i32_e32 v15, 31, v14
	v_lshl_add_u64 v[14:15], v[14:15], 4, s[6:7]
	s_add_i32 s12, s3, 0xc0
	global_load_dwordx4 v[98:101], v[14:15], off nt
	v_or_b32_e32 v14, s12, v1
	v_ashrrev_i32_e32 v15, 31, v14
	v_lshl_add_u64 v[14:15], v[14:15], 4, s[6:7]
	s_add_i32 s12, s11, 64
	global_load_dwordx4 v[82:85], v[14:15], off nt
	v_or_b32_e32 v14, s12, v1
	v_ashrrev_i32_e32 v15, 31, v14
	v_lshl_add_u64 v[14:15], v[14:15], 4, s[4:5]
	s_add_i32 s12, s11, 0x80
	global_load_dwordx4 v[34:37], v[14:15], off
	v_or_b32_e32 v14, s12, v1
	s_add_i32 s12, s11, 0xc0
	v_or_b32_e32 v16, s12, v1
	s_add_i32 s12, s11, 0x100
	v_or_b32_e32 v18, s12, v1
	s_add_i32 s12, s11, 0x140
	v_ashrrev_i32_e32 v15, 31, v14
	v_ashrrev_i32_e32 v17, 31, v16
	v_or_b32_e32 v20, s12, v1
	v_lshl_add_u64 v[14:15], v[14:15], 4, s[4:5]
	v_lshl_add_u64 v[16:17], v[16:17], 4, s[4:5]
	v_ashrrev_i32_e32 v21, 31, v20
	s_add_i32 s12, s11, 0x180
	global_load_dwordx4 v[30:33], v[14:15], off
	global_load_dwordx4 v[26:29], v[16:17], off
	v_lshl_add_u64 v[14:15], v[20:21], 4, s[4:5]
	v_or_b32_e32 v20, s12, v1
	v_ashrrev_i32_e32 v21, 31, v20
	s_add_i32 s12, s11, 0x1c0
	v_lshl_add_u64 v[38:39], v[20:21], 4, s[4:5]
	v_or_b32_e32 v20, s12, v1
	v_ashrrev_i32_e32 v21, 31, v20
	s_addk_i32 s11, 0x200
	v_lshl_add_u64 v[40:41], v[20:21], 4, s[4:5]
	v_or_b32_e32 v20, s11, v1
	v_ashrrev_i32_e32 v21, 31, v20
	s_add_i32 s11, s3, 0x100
	v_lshl_add_u64 v[42:43], v[20:21], 4, s[4:5]
	v_or_b32_e32 v20, s11, v1
	s_add_i32 s11, s3, 0x140
	v_or_b32_e32 v16, s11, v1
	v_ashrrev_i32_e32 v17, 31, v16
	s_add_i32 s11, s3, 0x180
	v_lshl_add_u64 v[46:47], v[16:17], 4, s[6:7]
	v_or_b32_e32 v16, s11, v1
	v_ashrrev_i32_e32 v17, 31, v16
	s_add_i32 s11, s3, 0x1c0
	v_lshl_add_u64 v[48:49], v[16:17], 4, s[6:7]
	v_or_b32_e32 v16, s11, v1
	v_ashrrev_i32_e32 v17, 31, v16
	s_add_i32 s11, s3, 0x200
	v_lshl_add_u64 v[50:51], v[16:17], 4, s[6:7]
	v_or_b32_e32 v16, s11, v1
	v_ashrrev_i32_e32 v17, 31, v16
	s_add_i32 s11, s3, 0x240
	v_lshl_add_u64 v[52:53], v[16:17], 4, s[6:7]
	v_or_b32_e32 v16, s11, v1
	v_ashrrev_i32_e32 v17, 31, v16
	s_add_i32 s11, s3, 0x280
	v_ashrrev_i32_e32 v19, 31, v18
	v_ashrrev_i32_e32 v21, 31, v20
	v_lshl_add_u64 v[66:67], v[16:17], 4, s[6:7]
	v_or_b32_e32 v16, s11, v1
	v_lshl_add_u64 v[18:19], v[18:19], 4, s[4:5]
	v_lshl_add_u64 v[44:45], v[20:21], 4, s[6:7]
	v_ashrrev_i32_e32 v17, 31, v16
	s_add_i32 s11, s3, 0x2c0
	global_load_dwordx4 v[22:25], v[18:19], off
	v_lshl_add_u64 v[86:87], v[16:17], 4, s[6:7]
	v_or_b32_e32 v16, s11, v1
	s_add_i32 s11, s3, 0x300
	global_load_dwordx4 v[18:21], v[14:15], off
	global_load_dwordx4 v[62:65], v[44:45], off nt
	v_lshlrev_b32_e32 v14, 4, v0
	s_waitcnt vmcnt(12)
	ds_write_b128 v14, v[6:9]
	v_or_b32_e32 v6, s11, v1
	v_ashrrev_i32_e32 v7, 31, v6
	s_add_i32 s11, s3, 0x340
	v_lshl_add_u64 v[142:143], v[6:7], 4, s[6:7]
	v_or_b32_e32 v6, s11, v1
	v_ashrrev_i32_e32 v7, 31, v6
	s_add_i32 s11, s3, 0x380
	v_lshl_add_u64 v[146:147], v[6:7], 4, s[6:7]
	v_or_b32_e32 v6, s11, v1
	v_ashrrev_i32_e32 v17, 31, v16
	v_ashrrev_i32_e32 v7, 31, v6
	v_lshl_add_u64 v[88:89], v[16:17], 4, s[6:7]
	s_waitcnt vmcnt(9)
	ds_write_b128 v14, v[10:13] offset:8192
	global_load_dwordx4 v[14:17], v[38:39], off
	global_load_dwordx4 v[10:13], v[40:41], off
	v_lshl_add_u64 v[38:39], v[6:7], 4, s[6:7]
	global_load_dwordx4 v[6:9], v[42:43], off
	global_load_dwordx4 v[94:97], v[46:47], off nt
	global_load_dwordx4 v[78:81], v[48:49], off nt
	global_load_dwordx4 v[74:77], v[50:51], off nt
	global_load_dwordx4 v[70:73], v[52:53], off nt
	s_add_i32 s11, s3, 0x3c0
	v_or_b32_e32 v40, s11, v1
	v_ashrrev_i32_e32 v41, 31, v40
	v_mfma_f32_16x16x32_f16 v[102:105], v[58:61], v[2:5], 0
	v_lshl_add_u64 v[40:41], v[40:41], 4, s[6:7]
	global_load_dwordx4 v[66:69], v[66:67], off nt
	s_nop 0
	global_load_dwordx4 v[90:93], v[86:87], off nt
	s_nop 0
	global_load_dwordx4 v[86:89], v[88:89], off nt
	s_nop 0
	global_load_dwordx4 v[50:53], v[142:143], off nt
	global_load_dwordx4 v[46:49], v[146:147], off nt
	global_load_dwordx4 v[42:45], v[38:39], off nt
	s_nop 0
	global_load_dwordx4 v[38:41], v[40:41], off nt
	s_waitcnt vmcnt(22)
	v_mfma_f32_16x16x32_f16 v[106:109], v[54:57], v[2:5], 0
	s_mov_b32 s11, 0x7f000000
	v_mov_b32_e32 v159, 0
	v_mov_b32_e32 v171, 0
	s_waitcnt vmcnt(21)
	v_mfma_f32_16x16x32_f16 v[110:113], v[98:101], v[2:5], 0
	v_mov_b32_e32 v173, 0
	v_mov_b32_e32 v197, 0
	v_mov_b32_e32 v195, 0
	s_waitcnt vmcnt(20)
	v_mfma_f32_16x16x32_f16 v[114:117], v[82:85], v[2:5], 0
	v_mov_b32_e32 v199, 0
	v_min_i32_e32 v102, v102, v103
	v_min_i32_e32 v103, v104, v105
	v_min_i32_e32 v104, v106, v107
	v_min_i32_e32 v105, v108, v109
	v_min_i32_e32 v154, v110, v111
	v_min3_i32 v102, v102, v103, v104
	v_min_i32_e32 v155, v112, v113
	v_min_i32_e32 v114, v114, v115
	v_min3_i32 v102, v102, v105, v154
	s_waitcnt vmcnt(19)
	v_mfma_f32_16x16x32_f16 v[118:121], v[58:61], v[34:37], 0
	v_min_i32_e32 v115, v116, v117
	v_min3_i32 v102, v102, v155, v114
	v_min3_i32 v158, v102, v115, s11
	v_mfma_f32_16x16x32_f16 v[122:125], v[54:57], v[34:37], 0
	v_mov_b32_e32 v204, 0
	s_add_i32 s12, s3, 0x400
	v_mov_b32_e32 v205, 0
	v_mfma_f32_16x16x32_f16 v[126:129], v[98:101], v[34:37], 0
	v_mov_b32_e32 v220, 0
	v_mfma_f32_16x16x32_f16 v[130:133], v[82:85], v[34:37], 0
	s_waitcnt vmcnt(18)
	v_mfma_f32_16x16x32_f16 v[134:137], v[58:61], v[30:33], 0
	v_mfma_f32_16x16x32_f16 v[138:141], v[54:57], v[30:33], 0
	v_mfma_f32_16x16x32_f16 v[142:145], v[98:101], v[30:33], 0
	v_mfma_f32_16x16x32_f16 v[146:149], v[82:85], v[30:33], 0
	s_nop 0
	v_min_i32_e32 v102, v118, v119
	v_min_i32_e32 v103, v120, v121
	v_min_i32_e32 v104, v122, v123
	v_min_i32_e32 v105, v124, v125
	v_min_i32_e32 v114, v126, v127
	v_min3_i32 v102, v102, v103, v104
	v_min_i32_e32 v115, v128, v129
	v_min_i32_e32 v116, v130, v131
	v_min3_i32 v102, v102, v105, v114
	v_min_i32_e32 v117, v132, v133
	v_min3_i32 v102, v102, v115, v116
	s_waitcnt vmcnt(17)
	v_mfma_f32_16x16x32_f16 v[150:153], v[58:61], v[26:29], 0
	v_min3_i32 v170, v102, v117, s11
	v_mfma_f32_16x16x32_f16 v[106:109], v[54:57], v[26:29], 0
	v_mfma_f32_16x16x32_f16 v[110:113], v[98:101], v[26:29], 0
	v_mfma_f32_16x16x32_f16 v[154:157], v[82:85], v[26:29], 0
	s_nop 0
	v_min_i32_e32 v114, v134, v135
	v_min_i32_e32 v115, v136, v137
	v_min_i32_e32 v116, v138, v139
	v_min_i32_e32 v117, v140, v141
	v_min_i32_e32 v122, v142, v143
	v_min3_i32 v114, v114, v115, v116
	v_min_i32_e32 v123, v144, v145
	v_min_i32_e32 v124, v146, v147
	v_min3_i32 v114, v114, v117, v122
	v_min_i32_e32 v125, v148, v149
	v_min3_i32 v114, v114, v123, v124
	s_waitcnt vmcnt(16)
	v_mfma_f32_16x16x32_f16 v[160:163], v[58:61], v[22:25], 0
	v_min3_i32 v172, v114, v125, s11
	v_mfma_f32_16x16x32_f16 v[164:167], v[54:57], v[22:25], 0
	v_mfma_f32_16x16x32_f16 v[118:121], v[98:101], v[22:25], 0
	v_mfma_f32_16x16x32_f16 v[128:131], v[82:85], v[22:25], 0
	s_nop 0
	v_min_i32_e32 v110, v110, v111
	s_waitcnt vmcnt(15)
	v_mfma_f32_16x16x32_f16 v[174:177], v[58:61], v[18:21], 0
	v_min_i32_e32 v111, v112, v113
	v_min_i32_e32 v112, v154, v155
	v_min_i32_e32 v113, v156, v157
	s_waitcnt vmcnt(13)
	v_mfma_f32_16x16x32_f16 v[102:105], v[58:61], v[14:17], 0
	s_waitcnt vmcnt(12)
	v_mfma_f32_16x16x32_f16 v[134:137], v[58:61], v[10:13], 0
	s_waitcnt vmcnt(11)
	v_mfma_f32_16x16x32_f16 v[114:117], v[58:61], v[6:9], 0
	v_min_i32_e32 v58, v150, v151
	v_min_i32_e32 v59, v152, v153
	v_min_i32_e32 v60, v106, v107
	v_min_i32_e32 v61, v108, v109
	v_min3_i32 v58, v58, v59, v60
	v_min3_i32 v58, v58, v61, v110
	v_min3_i32 v58, v58, v111, v112
	v_mfma_f32_16x16x32_f16 v[178:181], v[54:57], v[18:21], 0
	v_min3_i32 v196, v58, v113, s11
	v_mfma_f32_16x16x32_f16 v[182:185], v[98:101], v[18:21], 0
	v_mfma_f32_16x16x32_f16 v[186:189], v[82:85], v[18:21], 0
	s_nop 0
	v_min_i32_e32 v110, v160, v161
	v_min_i32_e32 v111, v162, v163
	v_min_i32_e32 v112, v164, v165
	v_mfma_f32_16x16x32_f16 v[142:145], v[54:57], v[14:17], 0
	v_min_i32_e32 v113, v166, v167
	v_min_i32_e32 v118, v118, v119
	v_min_i32_e32 v119, v120, v121
	v_mfma_f32_16x16x32_f16 v[146:149], v[98:101], v[14:17], 0
	v_min_i32_e32 v120, v128, v129
	v_mfma_f32_16x16x32_f16 v[58:61], v[54:57], v[10:13], 0
	v_mfma_f32_16x16x32_f16 v[122:125], v[54:57], v[6:9], 0
	v_mfma_f32_16x16x32_f16 v[54:57], v[98:101], v[10:13], 0
	v_mfma_f32_16x16x32_f16 v[126:129], v[98:101], v[6:9], 0
	v_min3_i32 v99, v110, v111, v112
	v_min3_i32 v99, v99, v113, v118
	v_min_i32_e32 v98, v130, v131
	v_min3_i32 v99, v99, v119, v120
	v_mfma_f32_16x16x32_f16 v[106:109], v[82:85], v[14:17], 0
	v_min3_i32 v194, v99, v98, s11
	v_mfma_f32_16x16x32_f16 v[138:141], v[82:85], v[10:13], 0
	v_min_i32_e32 v98, v182, v183
	v_min_i32_e32 v99, v184, v185
	v_min_i32_e32 v100, v186, v187
	v_mfma_f32_16x16x32_f16 v[130:133], v[82:85], v[6:9], 0
	v_min_i32_e32 v82, v174, v175
	v_min_i32_e32 v83, v176, v177
	v_min_i32_e32 v84, v178, v179
	v_min_i32_e32 v85, v180, v181
	v_min3_i32 v82, v82, v83, v84
	v_min3_i32 v82, v82, v85, v98
	v_min_i32_e32 v101, v188, v189
	v_min3_i32 v82, v82, v99, v100
	v_min3_i32 v198, v82, v101, s11
	v_mfma_f32_16x16x32_f16 v[150:153], v[62:65], v[2:5], 0
	v_min_i32_e32 v82, v102, v103
	v_min_i32_e32 v83, v104, v105
	v_min_i32_e32 v84, v142, v143
	v_min_i32_e32 v85, v144, v145
	v_min_i32_e32 v98, v146, v147
	v_min3_i32 v82, v82, v83, v84
	v_min_i32_e32 v99, v148, v149
	v_min_i32_e32 v100, v106, v107
	v_min3_i32 v82, v82, v85, v98
	v_min_i32_e32 v101, v108, v109
	v_min3_i32 v82, v82, v99, v100
	v_min3_i32 v203, v82, v101, s11
	v_mfma_f32_16x16x32_f16 v[162:165], v[62:65], v[34:37], 0
	v_min_i32_e32 v58, v58, v59
	v_min_i32_e32 v59, v60, v61
	v_min_i32_e32 v54, v54, v55
	v_mfma_f32_16x16x32_f16 v[166:169], v[62:65], v[30:33], 0
	v_min_i32_e32 v55, v56, v57
	v_min_i32_e32 v56, v138, v139
	v_min_i32_e32 v57, v140, v141
	v_mfma_f32_16x16x32_f16 v[154:157], v[62:65], v[26:29], 0
	v_mfma_f32_16x16x32_f16 v[110:113], v[62:65], v[22:25], 0
	v_mfma_f32_16x16x32_f16 v[118:121], v[62:65], v[18:21], 0
	v_mfma_f32_16x16x32_f16 v[102:105], v[62:65], v[14:17], 0
	v_mfma_f32_16x16x32_f16 v[106:109], v[62:65], v[10:13], 0
	v_mfma_f32_16x16x32_f16 v[98:101], v[62:65], v[6:9], 0
	v_min_i32_e32 v62, v134, v135
	v_min_i32_e32 v63, v136, v137
	v_min3_i32 v58, v62, v63, v58
	v_min3_i32 v54, v58, v59, v54
	v_min3_i32 v54, v54, v55, v56
	v_min3_i32 v202, v54, v57, s11
	v_mov_b32_e32 v54, 0
	s_waitcnt vmcnt(10)
	v_mfma_f32_16x16x32_f16 v[174:177], v[94:97], v[2:5], 0
	v_add_u32_e32 v60, v1, v54
	v_add_u32_e32 v54, s12, v60
	s_add_i32 s12, s3, 0x440
	v_add_u32_e32 v56, s12, v60
	s_add_i32 s12, s3, 0x480
	v_add_u32_e32 v58, s12, v60
	s_add_i32 s12, s3, 0x4c0
	v_ashrrev_i32_e32 v55, 31, v54
	v_ashrrev_i32_e32 v57, 31, v56
	v_ashrrev_i32_e32 v59, 31, v58
	v_add_u32_e32 v60, s12, v60
	s_waitcnt vmcnt(9)
	v_mfma_f32_16x16x32_f16 v[134:137], v[78:81], v[2:5], 0
	v_lshl_add_u64 v[54:55], v[54:55], 4, s[6:7]
	v_lshl_add_u64 v[56:57], v[56:57], 4, s[6:7]
	v_lshl_add_u64 v[58:59], v[58:59], 4, s[6:7]
	s_waitcnt vmcnt(8)
	v_mfma_f32_16x16x32_f16 v[178:181], v[74:77], v[2:5], 0
	v_ashrrev_i32_e32 v61, 31, v60
	v_lshl_add_u64 v[138:139], v[60:61], 4, s[6:7]
	global_load_dwordx4 v[82:85], v[54:55], off nt
	global_load_dwordx4 v[62:65], v[56:57], off nt
	s_nop 0
	global_load_dwordx4 v[58:61], v[58:59], off nt
	s_nop 0
	global_load_dwordx4 v[54:57], v[138:139], off nt
	v_mfma_f32_16x16x32_f16 v[182:185], v[94:97], v[34:37], 0
	v_min_i32_e32 v114, v114, v115
	v_min_i32_e32 v115, v116, v117
	v_min_i32_e32 v116, v122, v123
	v_min_i32_e32 v117, v124, v125
	v_min_i32_e32 v122, v126, v127
	v_min3_i32 v114, v114, v115, v116
	v_min_i32_e32 v123, v128, v129
	v_min_i32_e32 v124, v130, v131
	v_min3_i32 v114, v114, v117, v122
	v_min_i32_e32 v125, v132, v133
	v_min3_i32 v114, v114, v123, v124
	v_mfma_f32_16x16x32_f16 v[206:209], v[78:81], v[34:37], 0
	v_min3_i32 v218, v114, v125, s11
	s_add_i32 s11, s3, 0x500
	s_mov_b32 s12, 0x2aaaaaab
	v_mfma_f32_16x16x32_f16 v[212:215], v[74:77], v[34:37], 0
	s_nop 0
	v_min3_i32 v114, v150, v151, v158
	v_min3_i32 v114, v152, v153, v114
	v_min3_i32 v114, v174, v175, v114
	v_min3_i32 v130, v176, v177, v114
	v_min3_i32 v130, v134, v135, v130
	v_min3_i32 v130, v136, v137, v130
	v_min3_i32 v130, v178, v179, v130
	v_min3_i32 v219, v180, v181, v130
	v_cmp_ge_i32_e32 vcc, v219, v158
	v_mfma_f32_16x16x32_f16 v[224:227], v[94:97], v[30:33], 0
	s_nop 0
	v_cndmask_b32_e32 v221, 1, v159, vcc
	v_mfma_f32_16x16x32_f16 v[228:231], v[78:81], v[30:33], 0
	v_mfma_f32_16x16x32_f16 v[232:235], v[74:77], v[30:33], 0
	s_nop 0
	v_min3_i32 v130, v162, v163, v170
	v_min3_i32 v130, v164, v165, v130
	v_min3_i32 v130, v182, v183, v130
	v_min3_i32 v130, v184, v185, v130
	v_min3_i32 v134, v206, v207, v130
	v_mfma_f32_16x16x32_f16 v[236:239], v[94:97], v[26:29], 0
	v_mfma_f32_16x16x32_f16 v[186:189], v[94:97], v[22:25], 0
	v_mfma_f32_16x16x32_f16 v[146:149], v[94:97], v[18:21], 0
	v_mfma_f32_16x16x32_f16 v[138:141], v[94:97], v[14:17], 0
	v_mfma_f32_16x16x32_f16 v[142:145], v[94:97], v[10:13], 0
	v_mfma_f32_16x16x32_f16 v[126:129], v[94:97], v[6:9], 0
	v_mfma_f32_16x16x32_f16 v[94:97], v[78:81], v[26:29], 0
	v_mfma_f32_16x16x32_f16 v[190:193], v[78:81], v[22:25], 0
	v_mfma_f32_16x16x32_f16 v[174:177], v[78:81], v[18:21], 0
	v_mfma_f32_16x16x32_f16 v[158:161], v[78:81], v[14:17], 0
	v_mfma_f32_16x16x32_f16 v[162:165], v[78:81], v[10:13], 0
	v_mfma_f32_16x16x32_f16 v[130:133], v[78:81], v[6:9], 0
	v_min3_i32 v78, v208, v209, v134
	v_min3_i32 v78, v212, v213, v78
	v_min3_i32 v217, v214, v215, v78
	v_cmp_ge_i32_e32 vcc, v217, v170
	v_mfma_f32_16x16x32_f16 v[122:125], v[74:77], v[26:29], 0
	s_nop 0
	v_cndmask_b32_e32 v222, 1, v171, vcc
	v_mfma_f32_16x16x32_f16 v[114:117], v[74:77], v[22:25], 0
	v_min3_i32 v78, v166, v167, v172
	v_min3_i32 v78, v168, v169, v78
	v_min3_i32 v78, v224, v225, v78
	v_min3_i32 v134, v226, v227, v78
	v_min3_i32 v134, v228, v229, v134
	v_min3_i32 v134, v230, v231, v134
	v_min3_i32 v134, v232, v233, v134
	v_min3_i32 v211, v234, v235, v134
	v_cmp_ge_i32_e32 vcc, v211, v172
	v_mfma_f32_16x16x32_f16 v[182:185], v[74:77], v[18:21], 0
	s_nop 0
	v_cndmask_b32_e32 v213, 1, v173, vcc
	v_mfma_f32_16x16x32_f16 v[178:181], v[74:77], v[14:17], 0
	v_mfma_f32_16x16x32_f16 v[78:81], v[74:77], v[10:13], 0
	v_mfma_f32_16x16x32_f16 v[150:153], v[74:77], v[6:9], 0
	v_min3_i32 v74, v154, v155, v196
	v_min3_i32 v74, v156, v157, v74
	v_min3_i32 v74, v236, v237, v74
	v_min3_i32 v74, v238, v239, v74
	v_min3_i32 v74, v94, v95, v74
	v_min3_i32 v74, v96, v97, v74
	v_min3_i32 v74, v122, v123, v74
	v_min3_i32 v212, v124, v125, v74
	v_cmp_ge_i32_e32 vcc, v212, v196
	s_waitcnt vmcnt(11)
	v_mfma_f32_16x16x32_f16 v[166:169], v[70:73], v[2:5], 0
	v_cndmask_b32_e32 v214, 1, v197, vcc
	v_mfma_f32_16x16x32_f16 v[170:173], v[70:73], v[34:37], 0
	v_min3_i32 v74, v110, v111, v194
	v_min3_i32 v74, v112, v113, v74
	v_min3_i32 v74, v186, v187, v74
	v_min3_i32 v74, v188, v189, v74
	v_min3_i32 v74, v190, v191, v74
	v_min3_i32 v74, v192, v193, v74
	v_min3_i32 v74, v114, v115, v74
	v_min3_i32 v215, v116, v117, v74
	v_cmp_ge_i32_e32 vcc, v215, v194
	v_mfma_f32_16x16x32_f16 v[154:157], v[70:73], v[30:33], 0
	s_nop 0
	v_cndmask_b32_e32 v216, 1, v195, vcc
	v_mfma_f32_16x16x32_f16 v[134:137], v[70:73], v[26:29], 0
	v_min3_i32 v74, v118, v119, v198
	v_min3_i32 v74, v120, v121, v74
	v_mfma_f32_16x16x32_f16 v[122:125], v[70:73], v[22:25], 0
	v_mfma_f32_16x16x32_f16 v[94:97], v[70:73], v[18:21], 0
	v_mfma_f32_16x16x32_f16 v[110:113], v[70:73], v[14:17], 0
	v_mfma_f32_16x16x32_f16 v[114:117], v[70:73], v[10:13], 0
	v_mfma_f32_16x16x32_f16 v[118:121], v[70:73], v[6:9], 0
	v_min3_i32 v70, v146, v147, v74
	v_min3_i32 v70, v148, v149, v70
	v_min3_i32 v70, v174, v175, v70
	v_min3_i32 v70, v176, v177, v70
	v_min3_i32 v70, v182, v183, v70
	v_min3_i32 v223, v184, v185, v70
	v_cmp_ge_i32_e32 vcc, v223, v198
	s_waitcnt vmcnt(10)
	v_mfma_f32_16x16x32_f16 v[186:189], v[66:69], v[2:5], 0
	v_cndmask_b32_e32 v244, 1, v199, vcc
	v_mfma_f32_16x16x32_f16 v[190:193], v[66:69], v[34:37], 0
	v_min3_i32 v70, v102, v103, v203
	v_min3_i32 v70, v104, v105, v70
	v_min3_i32 v70, v138, v139, v70
	v_min3_i32 v70, v140, v141, v70
	v_min3_i32 v70, v158, v159, v70
	v_min3_i32 v70, v160, v161, v70
	v_min3_i32 v70, v178, v179, v70
	v_min3_i32 v245, v180, v181, v70
	v_cmp_ge_i32_e32 vcc, v245, v203
	v_mfma_f32_16x16x32_f16 v[224:227], v[66:69], v[30:33], 0
	s_nop 0
	v_cndmask_b32_e32 v246, 1, v204, vcc
	v_mfma_f32_16x16x32_f16 v[198:201], v[66:69], v[26:29], 0
	v_min3_i32 v70, v106, v107, v202
	v_min3_i32 v70, v108, v109, v70
	v_min3_i32 v70, v142, v143, v70
	v_mfma_f32_16x16x32_f16 v[158:161], v[66:69], v[22:25], 0
	v_min3_i32 v70, v144, v145, v70
	v_min3_i32 v70, v162, v163, v70
	v_min3_i32 v70, v164, v165, v70
	v_mfma_f32_16x16x32_f16 v[146:149], v[66:69], v[18:21], 0
	v_min3_i32 v70, v78, v79, v70
	v_min3_i32 v247, v80, v81, v70
	v_cmp_ge_i32_e32 vcc, v247, v202
	v_mfma_f32_16x16x32_f16 v[138:141], v[66:69], v[14:17], 0
	s_nop 0
	v_cndmask_b32_e32 v248, 1, v205, vcc
	v_mfma_f32_16x16x32_f16 v[106:109], v[66:69], v[10:13], 0
	v_mfma_f32_16x16x32_f16 v[102:105], v[66:69], v[6:9], 0
	v_mov_b32_e32 v66, 0
	s_nop 0
	v_add_u32_e32 v72, v1, v66
	v_add_u32_e32 v66, s11, v72
	s_add_i32 s11, s3, 0x540
	v_add_u32_e32 v68, s11, v72
	s_add_i32 s11, s3, 0x580
	v_add_u32_e32 v70, s11, v72
	s_addk_i32 s3, 0x5c0
	v_ashrrev_i32_e32 v67, 31, v66
	v_ashrrev_i32_e32 v69, 31, v68
	v_ashrrev_i32_e32 v71, 31, v70
	v_add_u32_e32 v72, s3, v72
	s_waitcnt vmcnt(9)
	v_mfma_f32_16x16x32_f16 v[178:181], v[90:93], v[2:5], 0
	v_lshl_add_u64 v[66:67], v[66:67], 4, s[6:7]
	v_lshl_add_u64 v[68:69], v[68:69], 4, s[6:7]
	v_lshl_add_u64 v[70:71], v[70:71], 4, s[6:7]
	s_waitcnt vmcnt(8)
	v_mfma_f32_16x16x32_f16 v[194:197], v[86:89], v[2:5], 0
	v_ashrrev_i32_e32 v73, 31, v72
	v_lshl_add_u64 v[142:143], v[72:73], 4, s[6:7]
	global_load_dwordx4 v[78:81], v[66:67], off nt
	global_load_dwordx4 v[74:77], v[68:69], off nt
	s_nop 0
	global_load_dwordx4 v[70:73], v[70:71], off nt
	s_nop 0
	global_load_dwordx4 v[66:69], v[142:143], off nt
	v_mfma_f32_16x16x32_f16 v[228:231], v[90:93], v[34:37], 0
	v_min3_i32 v98, v98, v99, v218
	v_min3_i32 v98, v100, v101, v98
	v_min3_i32 v98, v126, v127, v98
	v_min3_i32 v98, v128, v129, v98
	v_min3_i32 v98, v130, v131, v98
	v_min3_i32 v98, v132, v133, v98
	v_min3_i32 v98, v150, v151, v98
	v_min3_i32 v249, v152, v153, v98
	v_cmp_ge_i32_e32 vcc, v249, v218
	v_mfma_f32_16x16x32_f16 v[232:235], v[86:89], v[34:37], 0
	s_mul_i32 s3, s15, 6
	v_cndmask_b32_e32 v218, 1, v220, vcc
	v_mfma_f32_16x16x32_f16 v[236:239], v[90:93], v[30:33], 0
	v_min3_i32 v98, v166, v167, v219
	s_mul_i32 s11, s2, 0x90
	v_mfma_f32_16x16x32_f16 v[206:209], v[90:93], v[26:29], 0
	v_mfma_f32_16x16x32_f16 v[182:185], v[90:93], v[22:25], 0
	v_mfma_f32_16x16x32_f16 v[174:177], v[90:93], v[18:21], 0
	v_mfma_f32_16x16x32_f16 v[162:165], v[90:93], v[14:17], 0
	v_mfma_f32_16x16x32_f16 v[142:145], v[90:93], v[10:13], 0
	v_mfma_f32_16x16x32_f16 v[126:129], v[90:93], v[6:9], 0
	v_min3_i32 v90, v168, v169, v98
	v_min3_i32 v90, v186, v187, v90
	v_min3_i32 v98, v188, v189, v90
	v_min3_i32 v98, v178, v179, v98
	v_min3_i32 v98, v180, v181, v98
	v_min3_i32 v98, v194, v195, v98
	v_min3_i32 v220, v196, v197, v98
	v_cmp_ge_i32_e32 vcc, v220, v219
	v_mfma_f32_16x16x32_f16 v[240:243], v[86:89], v[30:33], 0
	s_nop 0
	v_cndmask_b32_e32 v219, 2, v221, vcc
	v_mfma_f32_16x16x32_f16 v[90:93], v[86:89], v[26:29], 0
	v_min3_i32 v98, v170, v171, v217
	v_min3_i32 v98, v172, v173, v98
	v_min3_i32 v98, v190, v191, v98
	v_min3_i32 v98, v192, v193, v98
	v_min3_i32 v98, v228, v229, v98
	v_min3_i32 v98, v230, v231, v98
	v_min3_i32 v98, v232, v233, v98
	v_min3_i32 v221, v234, v235, v98
	v_cmp_ge_i32_e32 vcc, v221, v217
	v_mfma_f32_16x16x32_f16 v[202:205], v[86:89], v[22:25], 0
	s_nop 0
	v_cndmask_b32_e32 v217, 2, v222, vcc
	v_mfma_f32_16x16x32_f16 v[194:197], v[86:89], v[18:21], 0
	v_mfma_f32_16x16x32_f16 v[186:189], v[86:89], v[14:17], 0
	v_mfma_f32_16x16x32_f16 v[166:169], v[86:89], v[10:13], 0
	v_mfma_f32_16x16x32_f16 v[150:153], v[86:89], v[6:9], 0
	v_min3_i32 v86, v154, v155, v211
	v_min3_i32 v86, v156, v157, v86
	v_min3_i32 v86, v224, v225, v86
	v_min3_i32 v86, v226, v227, v86
	v_min3_i32 v86, v236, v237, v86
	v_min3_i32 v86, v238, v239, v86
	v_min3_i32 v86, v240, v241, v86
	v_min3_i32 v222, v242, v243, v86
	v_cmp_ge_i32_e32 vcc, v222, v211
	s_waitcnt vmcnt(11)
	v_mfma_f32_16x16x32_f16 v[170:173], v[50:53], v[2:5], 0
	v_cndmask_b32_e32 v211, 2, v213, vcc
	v_mfma_f32_16x16x32_f16 v[154:157], v[50:53], v[34:37], 0
	v_min3_i32 v86, v134, v135, v212
	v_min3_i32 v86, v136, v137, v86
	v_min3_i32 v86, v198, v199, v86
	v_min3_i32 v86, v200, v201, v86
	v_min3_i32 v86, v206, v207, v86
	v_min3_i32 v86, v208, v209, v86
	v_min3_i32 v86, v90, v91, v86
	v_min3_i32 v198, v92, v93, v86
	v_cmp_ge_i32_e32 vcc, v198, v212
	s_waitcnt vmcnt(10)
	v_mfma_f32_16x16x32_f16 v[134:137], v[46:49], v[2:5], 0
	v_cndmask_b32_e32 v199, 2, v214, vcc
	v_mfma_f32_16x16x32_f16 v[178:181], v[50:53], v[30:33], 0
	v_min3_i32 v122, v122, v123, v215
	v_min3_i32 v122, v124, v125, v122
	v_min3_i32 v122, v158, v159, v122
	v_min3_i32 v122, v160, v161, v122
	v_min3_i32 v122, v182, v183, v122
	v_min3_i32 v122, v184, v185, v122
	v_min3_i32 v122, v202, v203, v122
	v_min3_i32 v200, v204, v205, v122
	v_cmp_ge_i32_e32 vcc, v200, v215
	s_waitcnt vmcnt(9)
	v_mfma_f32_16x16x32_f16 v[158:161], v[42:45], v[2:5], 0
	v_cndmask_b32_e32 v201, 2, v216, vcc
	s_waitcnt vmcnt(8)
	v_mfma_f32_16x16x32_f16 v[182:185], v[38:41], v[2:5], 0
	v_min3_i32 v94, v94, v95, v223
	v_min3_i32 v94, v96, v97, v94
	v_min3_i32 v94, v146, v147, v94
	v_min3_i32 v94, v148, v149, v94
	v_min3_i32 v94, v174, v175, v94
	v_min3_i32 v94, v176, v177, v94
	v_min3_i32 v94, v194, v195, v94
	v_min3_i32 v202, v196, v197, v94
	v_cmp_ge_i32_e32 vcc, v202, v223
	v_mfma_f32_16x16x32_f16 v[146:149], v[46:49], v[34:37], 0
	s_nop 0
	v_cndmask_b32_e32 v203, 2, v244, vcc
	v_mfma_f32_16x16x32_f16 v[174:177], v[42:45], v[34:37], 0
	v_min3_i32 v94, v110, v111, v245
	v_min3_i32 v94, v112, v113, v94
	v_min3_i32 v94, v138, v139, v94
	v_min3_i32 v94, v140, v141, v94
	v_min3_i32 v94, v162, v163, v94
	v_min3_i32 v94, v164, v165, v94
	v_min3_i32 v94, v186, v187, v94
	v_min3_i32 v204, v188, v189, v94
	v_cmp_ge_i32_e32 vcc, v204, v245
	v_mfma_f32_16x16x32_f16 v[194:197], v[38:41], v[34:37], 0
	s_nop 0
	v_cndmask_b32_e32 v205, 2, v246, vcc
	v_mfma_f32_16x16x32_f16 v[110:113], v[46:49], v[30:33], 0
	v_min3_i32 v94, v114, v115, v247
	v_min3_i32 v94, v116, v117, v94
	v_min3_i32 v94, v106, v107, v94
	v_min3_i32 v94, v108, v109, v94
	v_min3_i32 v94, v142, v143, v94
	v_min3_i32 v94, v144, v145, v94
	v_min3_i32 v94, v166, v167, v94
	v_min3_i32 v206, v168, v169, v94
	v_cmp_ge_i32_e32 vcc, v206, v247
	v_mfma_f32_16x16x32_f16 v[190:193], v[50:53], v[26:29], 0
	s_nop 0
	v_cndmask_b32_e32 v207, 2, v248, vcc
	v_mfma_f32_16x16x32_f16 v[138:141], v[46:49], v[26:29], 0
	v_min3_i32 v114, v118, v119, v249
	v_min3_i32 v114, v120, v121, v114
	v_min3_i32 v102, v102, v103, v114
	v_min3_i32 v102, v104, v105, v102
	v_min3_i32 v102, v126, v127, v102
	v_min3_i32 v102, v128, v129, v102
	v_min3_i32 v102, v150, v151, v102
	v_min3_i32 v208, v152, v153, v102
	v_cmp_ge_i32_e32 vcc, v208, v249
	v_mfma_f32_16x16x32_f16 v[118:121], v[42:45], v[30:33], 0
	s_nop 0
	v_cndmask_b32_e32 v209, 2, v218, vcc
	v_mfma_f32_16x16x32_f16 v[126:129], v[38:41], v[30:33], 0
	v_min3_i32 v102, v170, v171, v220
	v_min3_i32 v102, v172, v173, v102
	v_min3_i32 v102, v134, v135, v102
	v_min3_i32 v102, v136, v137, v102
	v_min3_i32 v102, v158, v159, v102
	v_min3_i32 v102, v160, v161, v102
	v_min3_i32 v102, v182, v183, v102
	v_min3_i32 v182, v184, v185, v102
	v_cmp_ge_i32_e32 vcc, v182, v220
	v_mfma_f32_16x16x32_f16 v[142:145], v[42:45], v[26:29], 0
	s_nop 0
	v_cndmask_b32_e32 v183, 3, v219, vcc
	v_mfma_f32_16x16x32_f16 v[150:153], v[38:41], v[26:29], 0
	v_min3_i32 v102, v154, v155, v221
	v_min3_i32 v102, v156, v157, v102
	v_min3_i32 v102, v146, v147, v102
	v_min3_i32 v134, v148, v149, v102
	v_min3_i32 v134, v174, v175, v134
	v_min3_i32 v134, v176, v177, v134
	v_min3_i32 v134, v194, v195, v134
	v_min3_i32 v174, v196, v197, v134
	v_cmp_ge_i32_e32 vcc, v174, v221
	v_mfma_f32_16x16x32_f16 v[130:133], v[50:53], v[22:25], 0
	s_nop 0
	v_cndmask_b32_e32 v175, 3, v217, vcc
	v_mfma_f32_16x16x32_f16 v[186:189], v[46:49], v[22:25], 0
	v_min3_i32 v134, v178, v179, v222
	v_min3_i32 v134, v180, v181, v134
	v_min3_i32 v110, v110, v111, v134
	v_min3_i32 v110, v112, v113, v110
	v_min3_i32 v110, v118, v119, v110
	v_min3_i32 v110, v120, v121, v110
	v_min3_i32 v110, v126, v127, v110
	v_min3_i32 v176, v128, v129, v110
	v_cmp_ge_i32_e32 vcc, v176, v222
	v_mfma_f32_16x16x32_f16 v[166:169], v[42:45], v[22:25], 0
	s_nop 0
	v_cndmask_b32_e32 v177, 3, v211, vcc
	v_mfma_f32_16x16x32_f16 v[170:173], v[38:41], v[22:25], 0
	s_nop 0
	v_min3_i32 v118, v190, v191, v198
	v_mfma_f32_16x16x32_f16 v[162:165], v[38:41], v[18:21], 0
	v_mfma_f32_16x16x32_f16 v[146:149], v[38:41], v[14:17], 0
	v_mfma_f32_16x16x32_f16 v[126:129], v[38:41], v[10:13], 0
	v_mfma_f32_16x16x32_f16 v[110:113], v[38:41], v[6:9], 0
	v_min3_i32 v38, v192, v193, v118
	v_min3_i32 v38, v138, v139, v38
	v_min3_i32 v38, v140, v141, v38
	v_min3_i32 v38, v142, v143, v38
	v_min3_i32 v38, v144, v145, v38
	v_min3_i32 v38, v150, v151, v38
	v_min3_i32 v178, v152, v153, v38
	v_cmp_ge_i32_e32 vcc, v178, v198
	v_mfma_f32_16x16x32_f16 v[98:101], v[50:53], v[18:21], 0
	s_nop 0
	v_cndmask_b32_e32 v179, 3, v199, vcc
	v_mfma_f32_16x16x32_f16 v[122:125], v[46:49], v[18:21], 0
	v_mfma_f32_16x16x32_f16 v[158:161], v[42:45], v[18:21], 0
	s_nop 0
	v_min3_i32 v38, v130, v131, v200
	v_min3_i32 v38, v132, v133, v38
	v_min3_i32 v38, v186, v187, v38
	v_min3_i32 v38, v188, v189, v38
	v_min3_i32 v38, v166, v167, v38
	v_min3_i32 v38, v168, v169, v38
	v_min3_i32 v38, v170, v171, v38
	v_min3_i32 v166, v172, v173, v38
	v_cmp_ge_i32_e32 vcc, v166, v200
	v_mfma_f32_16x16x32_f16 v[86:89], v[50:53], v[14:17], 0
	s_nop 0
	v_cndmask_b32_e32 v167, 3, v201, vcc
	v_mfma_f32_16x16x32_f16 v[106:109], v[46:49], v[14:17], 0
	v_mfma_f32_16x16x32_f16 v[114:117], v[42:45], v[14:17], 0
	s_nop 0
	v_min3_i32 v38, v98, v99, v202
	v_min3_i32 v38, v100, v101, v38
	v_min3_i32 v38, v122, v123, v38
	v_min3_i32 v38, v124, v125, v38
	v_min3_i32 v38, v158, v159, v38
	v_min3_i32 v38, v160, v161, v38
	v_min3_i32 v122, v162, v163, v38
	v_min3_i32 v158, v164, v165, v122
	v_cmp_ge_i32_e32 vcc, v158, v202
	v_mfma_f32_16x16x32_f16 v[90:93], v[50:53], v[10:13], 0
	s_nop 0
	v_cndmask_b32_e32 v159, 3, v203, vcc
	v_mfma_f32_16x16x32_f16 v[94:97], v[46:49], v[10:13], 0
	v_mfma_f32_16x16x32_f16 v[102:105], v[42:45], v[10:13], 0
	s_nop 0
	v_min3_i32 v86, v86, v87, v204
	v_min3_i32 v122, v88, v89, v86
	v_min3_i32 v106, v106, v107, v122
	v_min3_i32 v106, v108, v109, v106
	v_min3_i32 v114, v114, v115, v106
	v_min3_i32 v114, v116, v117, v114
	v_min3_i32 v114, v146, v147, v114
	v_min3_i32 v146, v148, v149, v114
	v_cmp_ge_i32_e32 vcc, v146, v204
	v_mfma_f32_16x16x32_f16 v[50:53], v[50:53], v[6:9], 0
	s_nop 0
	v_cndmask_b32_e32 v147, 3, v205, vcc
	v_mfma_f32_16x16x32_f16 v[46:49], v[46:49], v[6:9], 0
	v_mfma_f32_16x16x32_f16 v[42:45], v[42:45], v[6:9], 0
	s_nop 0
	v_min3_i32 v90, v90, v91, v206
	v_min3_i32 v90, v92, v93, v90
	v_min3_i32 v90, v94, v95, v90
	v_min3_i32 v94, v96, v97, v90
	v_min3_i32 v94, v102, v103, v94
	v_min3_i32 v94, v104, v105, v94
	v_min3_i32 v102, v126, v127, v94
	v_min3_i32 v148, v128, v129, v102
	v_cmp_ge_i32_e32 vcc, v148, v206
	s_waitcnt vmcnt(7)
	v_mfma_f32_16x16x32_f16 v[134:137], v[82:85], v[2:5], 0
	v_cndmask_b32_e32 v149, 3, v207, vcc
	v_mfma_f32_16x16x32_f16 v[138:141], v[82:85], v[34:37], 0
	v_mfma_f32_16x16x32_f16 v[142:145], v[82:85], v[30:33], 0
	v_mfma_f32_16x16x32_f16 v[150:153], v[82:85], v[26:29], 0
	v_mfma_f32_16x16x32_f16 v[154:157], v[82:85], v[22:25], 0
	v_mfma_f32_16x16x32_f16 v[130:133], v[82:85], v[18:21], 0
	v_mfma_f32_16x16x32_f16 v[118:121], v[82:85], v[14:17], 0
	v_mfma_f32_16x16x32_f16 v[98:101], v[82:85], v[10:13], 0
	v_mfma_f32_16x16x32_f16 v[38:41], v[82:85], v[6:9], 0
	s_waitcnt vmcnt(6)
	v_mfma_f32_16x16x32_f16 v[82:85], v[62:65], v[2:5], 0
	s_waitcnt vmcnt(5)
	v_mfma_f32_16x16x32_f16 v[86:89], v[58:61], v[2:5], 0
	s_waitcnt vmcnt(4)
	v_mfma_f32_16x16x32_f16 v[106:109], v[54:57], v[2:5], 0
	s_nop 0
	v_min3_i32 v50, v50, v51, v208
	v_min3_i32 v126, v52, v53, v50
	v_min3_i32 v46, v46, v47, v126
	v_min3_i32 v46, v48, v49, v46
	v_min3_i32 v42, v42, v43, v46
	v_min3_i32 v42, v44, v45, v42
	v_min3_i32 v42, v110, v111, v42
	v_min3_i32 v160, v112, v113, v42
	v_cmp_ge_i32_e32 vcc, v160, v208
	v_mfma_f32_16x16x32_f16 v[114:117], v[62:65], v[34:37], 0
	s_nop 0
	v_cndmask_b32_e32 v161, 3, v209, vcc
	v_mfma_f32_16x16x32_f16 v[122:125], v[58:61], v[34:37], 0
	v_mfma_f32_16x16x32_f16 v[90:93], v[54:57], v[34:37], 0
	s_nop 0
	v_min3_i32 v42, v134, v135, v182
	v_min3_i32 v42, v136, v137, v42
	v_min3_i32 v42, v82, v83, v42
	v_min3_i32 v42, v84, v85, v42
	v_min3_i32 v42, v86, v87, v42
	v_min3_i32 v42, v88, v89, v42
	v_min3_i32 v42, v106, v107, v42
	v_min3_i32 v134, v108, v109, v42
	v_cmp_ge_i32_e32 vcc, v134, v182
	v_mfma_f32_16x16x32_f16 v[94:97], v[62:65], v[30:33], 0
	s_nop 0
	v_cndmask_b32_e32 v135, 4, v183, vcc
	v_mfma_f32_16x16x32_f16 v[102:105], v[58:61], v[30:33], 0
	v_mfma_f32_16x16x32_f16 v[50:53], v[54:57], v[30:33], 0
	v_mfma_f32_16x16x32_f16 v[46:49], v[62:65], v[26:29], 0
	v_mfma_f32_16x16x32_f16 v[110:113], v[62:65], v[22:25], 0
	v_mfma_f32_16x16x32_f16 v[126:129], v[62:65], v[18:21], 0
	v_mfma_f32_16x16x32_f16 v[82:85], v[62:65], v[14:17], 0
	v_mfma_f32_16x16x32_f16 v[86:89], v[62:65], v[10:13], 0
	v_mfma_f32_16x16x32_f16 v[42:45], v[62:65], v[6:9], 0
	v_min3_i32 v62, v138, v139, v174
	v_min3_i32 v106, v140, v141, v62
	v_min3_i32 v106, v114, v115, v106
	v_min3_i32 v106, v116, v117, v106
	v_min3_i32 v114, v122, v123, v106
	v_min3_i32 v114, v124, v125, v114
	v_min3_i32 v90, v90, v91, v114
	v_min3_i32 v122, v92, v93, v90
	v_cmp_ge_i32_e32 vcc, v122, v174
	v_mfma_f32_16x16x32_f16 v[62:65], v[58:61], v[26:29], 0
	s_nop 0
	v_cndmask_b32_e32 v123, 4, v175, vcc
	v_mfma_f32_16x16x32_f16 v[106:109], v[54:57], v[26:29], 0
	s_nop 0
	v_min3_i32 v124, v142, v143, v176
	v_min3_i32 v124, v144, v145, v124
	v_min3_i32 v94, v94, v95, v124
	v_min3_i32 v124, v96, v97, v94
	v_min3_i32 v102, v102, v103, v124
	v_min3_i32 v102, v104, v105, v102
	v_min3_i32 v50, v50, v51, v102
	v_min3_i32 v124, v52, v53, v50
	v_cmp_ge_i32_e32 vcc, v124, v176
	v_mfma_f32_16x16x32_f16 v[90:93], v[58:61], v[22:25], 0
	s_nop 0
	v_cndmask_b32_e32 v125, 4, v177, vcc
	v_mfma_f32_16x16x32_f16 v[114:117], v[54:57], v[22:25], 0
	s_nop 0
	v_min3_i32 v136, v150, v151, v178
	v_min3_i32 v136, v152, v153, v136
	v_min3_i32 v46, v46, v47, v136
	v_min3_i32 v46, v48, v49, v46
	v_min3_i32 v62, v62, v63, v46
	v_min3_i32 v62, v64, v65, v62
	v_min3_i32 v62, v106, v107, v62
	v_min3_i32 v136, v108, v109, v62
	v_cmp_ge_i32_e32 vcc, v136, v178
	v_mfma_f32_16x16x32_f16 v[94:97], v[58:61], v[18:21], 0
	s_nop 0
	v_cndmask_b32_e32 v137, 4, v179, vcc
	v_mfma_f32_16x16x32_f16 v[46:49], v[54:57], v[18:21], 0
	s_nop 0
	v_min3_i32 v138, v154, v155, v166
	v_min3_i32 v138, v156, v157, v138
	v_min3_i32 v110, v110, v111, v138
	v_min3_i32 v110, v112, v113, v110
	v_min3_i32 v90, v90, v91, v110
	v_min3_i32 v90, v92, v93, v90
	v_min3_i32 v110, v114, v115, v90
	v_min3_i32 v138, v116, v117, v110
	v_cmp_ge_i32_e32 vcc, v138, v166
	v_mfma_f32_16x16x32_f16 v[102:105], v[58:61], v[14:17], 0
	v_mov_b32_e32 v154, 0
	v_cndmask_b32_e32 v139, 4, v167, vcc
	v_mfma_f32_16x16x32_f16 v[62:65], v[54:57], v[14:17], 0
	s_nop 0
	v_min3_i32 v114, v130, v131, v158
	v_min3_i32 v130, v132, v133, v114
	v_min3_i32 v126, v126, v127, v130
	v_min3_i32 v126, v128, v129, v126
	v_min3_i32 v94, v94, v95, v126
	v_min3_i32 v94, v96, v97, v94
	v_min3_i32 v46, v46, v47, v94
	v_min3_i32 v126, v48, v49, v46
	v_cmp_ge_i32_e32 vcc, v126, v158
	v_mfma_f32_16x16x32_f16 v[50:53], v[58:61], v[10:13], 0
	s_nop 0
	v_cndmask_b32_e32 v127, 4, v159, vcc
	v_mfma_f32_16x16x32_f16 v[106:109], v[54:57], v[10:13], 0
	s_nop 0
	v_min3_i32 v118, v118, v119, v146
	v_min3_i32 v118, v120, v121, v118
	v_min3_i32 v82, v82, v83, v118
	v_min3_i32 v118, v84, v85, v82
	v_min3_i32 v102, v102, v103, v118
	v_min3_i32 v102, v104, v105, v102
	v_min3_i32 v62, v62, v63, v102
	v_min3_i32 v102, v64, v65, v62
	v_cmp_ge_i32_e32 vcc, v102, v146
	v_mfma_f32_16x16x32_f16 v[58:61], v[58:61], v[6:9], 0
	v_and_b32_e32 v146, 7, v0
	v_cndmask_b32_e32 v103, 4, v147, vcc
	v_mfma_f32_16x16x32_f16 v[54:57], v[54:57], v[6:9], 0
	s_nop 0
	v_min3_i32 v98, v98, v99, v148
	v_min3_i32 v104, v100, v101, v98
	v_min3_i32 v86, v86, v87, v104
	v_min3_i32 v86, v88, v89, v86
	v_min3_i32 v50, v50, v51, v86
	v_min3_i32 v50, v52, v53, v50
	v_min3_i32 v50, v106, v107, v50
	v_min3_i32 v104, v108, v109, v50
	v_cmp_ge_i32_e32 vcc, v104, v148
	s_waitcnt vmcnt(3)
	v_mfma_f32_16x16x32_f16 v[90:93], v[78:81], v[2:5], 0
	v_cndmask_b32_e32 v105, 4, v149, vcc
	s_waitcnt vmcnt(2)
	v_mfma_f32_16x16x32_f16 v[110:113], v[74:77], v[2:5], 0
	s_waitcnt vmcnt(1)
	v_mfma_f32_16x16x32_f16 v[114:117], v[70:73], v[2:5], 0
	s_waitcnt vmcnt(0)
	v_mfma_f32_16x16x32_f16 v[2:5], v[66:69], v[2:5], 0
	s_nop 0
	v_min3_i32 v38, v38, v39, v160
	v_min3_i32 v38, v40, v41, v38
	v_min3_i32 v38, v42, v43, v38
	v_min3_i32 v42, v44, v45, v38
	v_min3_i32 v42, v58, v59, v42
	v_min3_i32 v42, v60, v61, v42
	v_min3_i32 v54, v54, v55, v42
	v_min3_i32 v106, v56, v57, v54
	v_cmp_ge_i32_e32 vcc, v106, v160
	v_mfma_f32_16x16x32_f16 v[46:49], v[78:81], v[34:37], 0
	s_nop 0
	v_cndmask_b32_e32 v107, 4, v161, vcc
	v_mfma_f32_16x16x32_f16 v[94:97], v[74:77], v[34:37], 0
	v_mfma_f32_16x16x32_f16 v[82:85], v[70:73], v[34:37], 0
	v_mfma_f32_16x16x32_f16 v[34:37], v[66:69], v[34:37], 0
	s_nop 0
	v_min3_i32 v54, v90, v91, v134
	v_min3_i32 v58, v92, v93, v54
	v_min3_i32 v58, v110, v111, v58
	v_min3_i32 v58, v112, v113, v58
	v_min3_i32 v90, v114, v115, v58
	v_min3_i32 v90, v116, v117, v90
	v_min3_i32 v2, v2, v3, v90
	v_min3_i32 v91, v4, v5, v2
	v_cmp_ge_i32_e32 vcc, v91, v134
	v_mfma_f32_16x16x32_f16 v[62:65], v[78:81], v[30:33], 0
	s_nop 0
	v_cndmask_b32_e32 v90, 5, v135, vcc
	v_add_u32_e32 v251, s3, v90
	v_lshl_or_b32 v90, v251, 2, v253
	ds_min_u64 v252, v[90:91] offset:16384
	v_mfma_f32_16x16x32_f16 v[98:101], v[74:77], v[30:33], 0
	v_mfma_f32_16x16x32_f16 v[86:89], v[70:73], v[30:33], 0
	v_mfma_f32_16x16x32_f16 v[30:33], v[66:69], v[30:33], 0
	s_nop 0
	v_min3_i32 v46, v46, v47, v122
	v_min3_i32 v46, v48, v49, v46
	v_min3_i32 v46, v94, v95, v46
	v_min3_i32 v92, v96, v97, v46
	v_min3_i32 v82, v82, v83, v92
	v_min3_i32 v82, v84, v85, v82
	v_min3_i32 v34, v34, v35, v82
	v_min3_i32 v93, v36, v37, v34
	v_cmp_ge_i32_e32 vcc, v93, v122
	v_mfma_f32_16x16x32_f16 v[50:53], v[78:81], v[26:29], 0
	s_nop 0
	v_cndmask_b32_e32 v92, 5, v123, vcc
	v_add_u32_e32 v251, s3, v92
	v_lshl_or_b32 v92, v251, 2, v253
	ds_min_u64 v252, v[92:93] offset:16512
	v_mfma_f32_16x16x32_f16 v[38:41], v[74:77], v[26:29], 0
	v_mfma_f32_16x16x32_f16 v[42:45], v[70:73], v[26:29], 0
	v_mfma_f32_16x16x32_f16 v[26:29], v[66:69], v[26:29], 0
	s_nop 0
	v_min3_i32 v62, v62, v63, v124
	v_min3_i32 v62, v64, v65, v62
	v_min3_i32 v62, v98, v99, v62
	v_min3_i32 v62, v100, v101, v62
	v_min3_i32 v86, v86, v87, v62
	v_min3_i32 v86, v88, v89, v86
	v_min3_i32 v30, v30, v31, v86
	v_min3_i32 v95, v32, v33, v30
	v_cmp_ge_i32_e32 vcc, v95, v124
	v_mfma_f32_16x16x32_f16 v[54:57], v[78:81], v[22:25], 0
	s_nop 0
	v_cndmask_b32_e32 v94, 5, v125, vcc
	v_add_u32_e32 v251, s3, v94
	v_lshl_or_b32 v94, v251, 2, v253
	ds_min_u64 v252, v[94:95] offset:16640
	v_mfma_f32_16x16x32_f16 v[58:61], v[74:77], v[22:25], 0
	v_mfma_f32_16x16x32_f16 v[2:5], v[70:73], v[22:25], 0
	v_mfma_f32_16x16x32_f16 v[22:25], v[66:69], v[22:25], 0
	s_nop 0
	v_min3_i32 v50, v50, v51, v136
	v_min3_i32 v50, v52, v53, v50
	v_min3_i32 v38, v38, v39, v50
	v_min3_i32 v38, v40, v41, v38
	v_min3_i32 v38, v42, v43, v38
	v_min3_i32 v38, v44, v45, v38
	v_min3_i32 v26, v26, v27, v38
	v_min3_i32 v51, v28, v29, v26
	v_cmp_ge_i32_e32 vcc, v51, v136
	v_mfma_f32_16x16x32_f16 v[46:49], v[78:81], v[18:21], 0
	s_nop 0
	v_cndmask_b32_e32 v50, 5, v137, vcc
	v_add_u32_e32 v251, s3, v50
	v_lshl_or_b32 v50, v251, 2, v253
	ds_min_u64 v252, v[50:51] offset:16768
	v_mfma_f32_16x16x32_f16 v[82:85], v[74:77], v[18:21], 0
	v_mfma_f32_16x16x32_f16 v[34:37], v[70:73], v[18:21], 0
	v_mfma_f32_16x16x32_f16 v[18:21], v[66:69], v[18:21], 0
	s_nop 0
	v_min3_i32 v42, v54, v55, v138
	v_min3_i32 v52, v56, v57, v42
	v_min3_i32 v52, v58, v59, v52
	v_min3_i32 v52, v60, v61, v52
	v_min3_i32 v2, v2, v3, v52
	v_min3_i32 v2, v4, v5, v2
	v_min3_i32 v2, v22, v23, v2
	v_min3_i32 v53, v24, v25, v2
	v_cmp_ge_i32_e32 vcc, v53, v138
	v_mfma_f32_16x16x32_f16 v[62:65], v[78:81], v[14:17], 0
	s_nop 0
	v_cndmask_b32_e32 v52, 5, v139, vcc
	v_add_u32_e32 v251, s3, v52
	v_lshl_or_b32 v52, v251, 2, v253
	ds_min_u64 v252, v[52:53] offset:16896
	v_mfma_f32_16x16x32_f16 v[30:33], v[74:77], v[14:17], 0
	v_mfma_f32_16x16x32_f16 v[86:89], v[70:73], v[14:17], 0
	v_mfma_f32_16x16x32_f16 v[14:17], v[66:69], v[14:17], 0
	s_nop 0
	v_min3_i32 v46, v46, v47, v126
	v_min3_i32 v46, v48, v49, v46
	v_min3_i32 v54, v82, v83, v46
	v_min3_i32 v54, v84, v85, v54
	v_min3_i32 v34, v34, v35, v54
	v_min3_i32 v34, v36, v37, v34
	v_min3_i32 v18, v18, v19, v34
	v_min3_i32 v19, v20, v21, v18
	v_cmp_ge_i32_e32 vcc, v19, v126
	v_mfma_f32_16x16x32_f16 v[38:41], v[78:81], v[10:13], 0
	s_nop 0
	v_cndmask_b32_e32 v18, 5, v127, vcc
	v_add_u32_e32 v251, s3, v18
	v_lshl_or_b32 v18, v251, 2, v253
	ds_min_u64 v252, v[18:19] offset:17024
	v_mfma_f32_16x16x32_f16 v[26:29], v[74:77], v[10:13], 0
	v_mfma_f32_16x16x32_f16 v[42:45], v[70:73], v[10:13], 0
	v_mfma_f32_16x16x32_f16 v[10:13], v[66:69], v[10:13], 0
	s_nop 0
	v_min3_i32 v20, v62, v63, v102
	v_min3_i32 v20, v64, v65, v20
	v_min3_i32 v20, v30, v31, v20
	v_min3_i32 v20, v32, v33, v20
	v_min3_i32 v20, v86, v87, v20
	v_min3_i32 v20, v88, v89, v20
	v_min3_i32 v14, v14, v15, v20
	v_min3_i32 v15, v16, v17, v14
	v_cmp_ge_i32_e32 vcc, v15, v102
	v_mfma_f32_16x16x32_f16 v[2:5], v[78:81], v[6:9], 0
	v_bfe_u32 v17, v0, 4, 2
	v_cndmask_b32_e32 v14, 5, v103, vcc
	v_add_u32_e32 v251, s3, v14
	v_lshl_or_b32 v14, v251, 2, v253
	ds_min_u64 v252, v[14:15] offset:17152
	v_mfma_f32_16x16x32_f16 v[22:25], v[74:77], v[6:9], 0
	v_mfma_f32_16x16x32_f16 v[46:49], v[70:73], v[6:9], 0
	v_mfma_f32_16x16x32_f16 v[6:9], v[66:69], v[6:9], 0
	s_nop 0
	v_min3_i32 v16, v38, v39, v104
	v_min3_i32 v16, v40, v41, v16
	v_min3_i32 v16, v26, v27, v16
	v_min3_i32 v2, v2, v3, v106
	v_min3_i32 v16, v28, v29, v16
	v_min3_i32 v2, v4, v5, v2
	v_min3_i32 v16, v42, v43, v16
	v_min3_i32 v2, v22, v23, v2
	v_lshlrev_b32_e32 v4, 3, v210
	v_min3_i32 v16, v44, v45, v16
	v_min3_i32 v2, v24, v25, v2
	v_min3_i32 v10, v10, v11, v16
	v_min3_i32 v2, v46, v47, v2
	v_min3_i32 v11, v12, v13, v10
	v_min3_i32 v2, v48, v49, v2
	v_cmp_ge_i32_e32 vcc, v11, v104
	v_min3_i32 v2, v6, v7, v2
	v_cndmask_b32_e32 v10, 5, v105, vcc
	v_add_u32_e32 v251, s3, v10
	v_lshl_or_b32 v10, v251, 2, v253
	ds_min_u64 v252, v[10:11] offset:17280
	v_min3_i32 v3, v8, v9, v2
	v_cmp_ge_i32_e32 vcc, v3, v106
	v_cndmask_b32_e32 v2, 5, v107, vcc
	v_add_u32_e32 v2, s3, v2
	v_bfe_u32 v10, v0, 3, 3
	s_lshl_b32 s3, s15, 3
	v_lshl_or_b32 v2, v2, 2, v17
	v_or_b32_e32 v151, s3, v10
	ds_min_u64 v4, v[2:3] offset:17408
	v_lshlrev_b32_e32 v2, 3, v151
	s_waitcnt lgkmcnt(0)
	s_barrier
	ds_read2st64_b32 v[4:5], v2 offset0:64 offset1:66
	s_add_i32 s2, s3, s11
	s_lshr_b32 s2, s2, 4
	s_add_i32 s2, s2, s8
	s_waitcnt lgkmcnt(0)
	v_ashrrev_i32_e32 v3, 2, v4
	v_mul_hi_i32 v6, v3, s12
	v_lshrrev_b32_e32 v7, 31, v6
	v_add_u32_e32 v6, v6, v7
	v_mul_lo_u32 v7, v6, -6
	v_mul_lo_u32 v6, v6, 24
	v_min_i32_e32 v6, 0xa5, v6
	v_add_lshl_u32 v7, v7, v3, 2
	v_bfe_u32 v3, v0, 2, 1
	v_add3_u32 v152, v6, v3, v7
	v_lshlrev_b32_e32 v6, 2, v4
	v_and_b32_e32 v4, 3, v0
	v_and_or_b32 v153, v6, 12, v4
	v_add_u32_e32 v6, s9, v152
	v_lshl_or_b32 v6, v6, 6, v153
	v_bitop3_b32 v7, s3, 15, v10 bitop3:0xc8
	v_lshl_or_b32 v8, s2, 6, v7
	v_ashrrev_i32_e32 v7, 31, v6
	v_lshl_add_u64 v[6:7], v[6:7], 4, s[6:7]
	v_ashrrev_i32_e32 v9, 31, v8
	v_lshl_add_u64 v[8:9], v[8:9], 4, s[4:5]
	global_load_dwordx4 v[126:129], v[6:7], off
	global_load_dwordx4 v[114:117], v[6:7], off offset:256
	global_load_dwordx4 v[130:133], v[6:7], off offset:2048
	global_load_dwordx4 v[118:121], v[6:7], off offset:2304
	global_load_dwordx4 v[134:137], v[8:9], off
	global_load_dwordx4 v[122:125], v[8:9], off offset:256
	global_load_dwordx4 v[102:105], v[6:7], off offset:512
	global_load_dwordx4 v[78:81], v[6:7], off offset:768
	global_load_dwordx4 v[106:109], v[6:7], off offset:2560
	global_load_dwordx4 v[82:85], v[6:7], off offset:2816
	v_ashrrev_i32_e32 v6, 2, v5
	v_mul_hi_i32 v7, v6, s12
	v_lshrrev_b32_e32 v11, 31, v7
	v_add_u32_e32 v7, v7, v11
	v_mul_lo_u32 v11, v7, -6
	v_mul_lo_u32 v7, v7, 24
	s_add_i32 s2, s3, 64
	v_min_i32_e32 v7, 0xa5, v7
	v_add_lshl_u32 v6, v11, v6, 2
	s_add_i32 s3, s2, s11
	v_add3_u32 v148, v7, v3, v6
	v_lshlrev_b32_e32 v5, 2, v5
	v_and_or_b32 v149, v5, 12, v4
	v_add_u32_e32 v5, s9, v148
	s_lshr_b32 s3, s3, 4
	v_lshl_or_b32 v6, v5, 6, v149
	s_add_i32 s3, s3, s8
	v_bitop3_b32 v5, s2, 15, v10 bitop3:0xc8
	v_lshl_or_b32 v10, s3, 6, v5
	v_ashrrev_i32_e32 v7, 31, v6
	v_ashrrev_i32_e32 v11, 31, v10
	v_lshl_add_u64 v[6:7], v[6:7], 4, s[6:7]
	v_lshl_add_u64 v[10:11], v[10:11], 4, s[4:5]
	global_load_dwordx4 v[142:145], v[8:9], off offset:512
	global_load_dwordx4 v[138:141], v[8:9], off offset:768
	global_load_dwordx4 v[90:93], v[6:7], off
	global_load_dwordx4 v[62:65], v[6:7], off offset:256
	global_load_dwordx4 v[94:97], v[6:7], off offset:2048
	global_load_dwordx4 v[66:69], v[6:7], off offset:2304
	global_load_dwordx4 v[38:41], v[6:7], off offset:512
	global_load_dwordx4 v[18:21], v[6:7], off offset:768
	global_load_dwordx4 v[42:45], v[6:7], off offset:2560
	global_load_dwordx4 v[22:25], v[6:7], off offset:2816
	global_load_dwordx4 v[110:113], v[10:11], off
	global_load_dwordx4 v[86:89], v[10:11], off offset:256
	global_load_dwordx4 v[54:57], v[10:11], off offset:512
	global_load_dwordx4 v[26:29], v[10:11], off offset:768
	s_cmpk_lt_u32 s10, 0x80
	s_cselect_b64 s[2:3], -1, 0
	s_cmpk_gt_u32 s10, 0x7f
	s_cbranch_scc1 .LBB1_4
	v_add_u32_e32 v2, 0x4000, v2
	ds_read_b32 v2, v2 offset:1024
	v_or_b32_e32 v147, 0x80, v151
	v_add_u32_e32 v5, s11, v147
	s_waitcnt lgkmcnt(0)
	v_ashrrev_i32_e32 v6, 2, v2
	v_mul_hi_i32 v7, v6, s12
	v_lshrrev_b32_e32 v8, 31, v7
	v_add_u32_e32 v7, v7, v8
	v_mul_lo_u32 v8, v7, -6
	v_mul_lo_u32 v7, v7, 24
	v_min_i32_e32 v7, 0xa5, v7
	v_add_lshl_u32 v6, v8, v6, 2
	v_add3_u32 v150, v7, v3, v6
	v_lshlrev_b32_e32 v2, 2, v2
	v_lshrrev_b32_e32 v3, 4, v5
	v_and_or_b32 v155, v2, 12, v4
	v_add_u32_e32 v2, s9, v150
	v_add_u32_e32 v3, s8, v3
	v_lshl_or_b32 v2, v2, 6, v155
	v_lshl_or_b32 v4, v3, 6, v151
	v_ashrrev_i32_e32 v3, 31, v2
	v_ashrrev_i32_e32 v5, 31, v4
	v_lshl_add_u64 v[2:3], v[2:3], 4, s[6:7]
	v_lshl_add_u64 v[50:51], v[4:5], 4, s[4:5]
	global_load_dwordx4 v[58:61], v[2:3], off
	global_load_dwordx4 v[46:49], v[2:3], off offset:256
	global_load_dwordx4 v[34:37], v[2:3], off offset:2048
	global_load_dwordx4 v[10:13], v[2:3], off offset:2304
	global_load_dwordx4 v[98:101], v[50:51], off
	global_load_dwordx4 v[74:77], v[50:51], off offset:256
	global_load_dwordx4 v[30:33], v[2:3], off offset:512
	global_load_dwordx4 v[14:17], v[2:3], off offset:768
	global_load_dwordx4 v[6:9], v[2:3], off offset:2560
	s_nop 0
	global_load_dwordx4 v[2:5], v[2:3], off offset:2816
	s_nop 0
	global_load_dwordx4 v[70:73], v[50:51], off offset:512
	s_nop 0
	global_load_dwordx4 v[50:53], v[50:51], off offset:768
	v_lshl_or_b32 v150, v150, 4, v155
	s_branch .LBB1_5

	.amdhsa_kernel _ZN12_GLOBAL__N_113search_kernelEPKfS1_PhPf
		.amdhsa_group_segment_fixed_size 18144
		.amdhsa_private_segment_fixed_size 0
		.amdhsa_kernarg_size 32
		.amdhsa_user_sgpr_count 2
		.amdhsa_user_sgpr_dispatch_ptr 0
		.amdhsa_user_sgpr_queue_ptr 0
		.amdhsa_user_sgpr_kernarg_segment_ptr 1
		.amdhsa_user_sgpr_dispatch_id 0
		.amdhsa_user_sgpr_kernarg_preload_length 0
		.amdhsa_user_sgpr_kernarg_preload_offset 0
		.amdhsa_user_sgpr_private_segment_size 0
		.amdhsa_uses_dynamic_stack 0
		.amdhsa_enable_private_segment 0
		.amdhsa_system_sgpr_workgroup_id_x 1
		.amdhsa_system_sgpr_workgroup_id_y 0
		.amdhsa_system_sgpr_workgroup_id_z 0
		.amdhsa_system_sgpr_workgroup_info 0
		.amdhsa_system_vgpr_workitem_id 0
		.amdhsa_next_free_vgpr 256
		.amdhsa_next_free_sgpr 20
		.amdhsa_accum_offset 256
		.amdhsa_reserve_vcc 1
		.amdhsa_float_round_mode_32 0
		.amdhsa_float_round_mode_16_64 0
		.amdhsa_float_denorm_mode_32 3
		.amdhsa_float_denorm_mode_16_64 3
		.amdhsa_dx10_clamp 1
		.amdhsa_ieee_mode 1
		.amdhsa_fp16_overflow 0
		.amdhsa_tg_split 0
		.amdhsa_exception_fp_ieee_invalid_op 0
		.amdhsa_exception_fp_denorm_src 0
		.amdhsa_exception_fp_ieee_div_zero 0
		.amdhsa_exception_fp_ieee_overflow 0
		.amdhsa_exception_fp_ieee_underflow 0
		.amdhsa_exception_fp_ieee_inexact 0
		.amdhsa_exception_int_div_zero 0
	.end_amdhsa_kernel

amdhsa.kernels:
  - .agpr_count:     0
    .args:
      - .actual_access:  read_only
        .address_space:  global
        .offset:         0
        .size:           8
        .value_kind:     global_buffer
      - .actual_access:  read_only
        .address_space:  global
        .offset:         8
        .size:           8
        .value_kind:     global_buffer
      - .actual_access:  write_only
        .address_space:  global
        .offset:         16
        .size:           8
        .value_kind:     global_buffer
    .group_segment_fixed_size: 26112
    .kernarg_segment_align: 8
    .kernarg_segment_size: 24
    .language:       OpenCL C
    .language_version:
      - 2
      - 0
    .max_flat_workgroup_size: 256
    .name:           _ZN12_GLOBAL__N_111prep_kernelEPKfS1_Ph
    .private_segment_fixed_size: 0
    .sgpr_count:     25
    .sgpr_spill_count: 0
    .symbol:         _ZN12_GLOBAL__N_111prep_kernelEPKfS1_Ph.kd
    .uniform_work_group_size: 1
    .uses_dynamic_stack: false
    .vgpr_count:     34
    .vgpr_spill_count: 0
    .wavefront_size: 64
  - .agpr_count:     0
    .args:
      - .actual_access:  read_only
        .address_space:  global
        .offset:         0
        .size:           8
        .value_kind:     global_buffer
      - .actual_access:  read_only
        .address_space:  global
        .offset:         8
        .size:           8
        .value_kind:     global_buffer
      - .address_space:  global
        .offset:         16
        .size:           8
        .value_kind:     global_buffer
      - .actual_access:  write_only
        .address_space:  global
        .offset:         24
        .size:           8
        .value_kind:     global_buffer
    .group_segment_fixed_size: 18144
    .kernarg_segment_align: 8
    .kernarg_segment_size: 32
    .language:       OpenCL C
    .language_version:
      - 2
      - 0
    .max_flat_workgroup_size: 512
    .name:           _ZN12_GLOBAL__N_113search_kernelEPKfS1_PhPf
    .private_segment_fixed_size: 0
    .sgpr_count:     26
    .sgpr_spill_count: 0
    .symbol:         _ZN12_GLOBAL__N_113search_kernelEPKfS1_PhPf.kd
    .uniform_work_group_size: 1
    .uses_dynamic_stack: false
    .vgpr_count:     256
    .vgpr_spill_count: 0
    .wavefront_size: 64
